# hand-written grid barriers (poll interval 4) + nt hint on the read-once adaLN weight stream of phase 0
# speedup vs baseline: 1.0100x; 1.0100x over previous
; __device__ __forceinline__ void p0a_mod_partials(Frame& F, const Args& A) {
;     ...
;     for (int u = gw; u < 1536; u += NGW) {
;         const int j = u / 384, r = u % 384, nc = r / 16, kc = r % 16, layer = j >> 1;
;         const float* W = ((j & 1) ? A.in[6] : A.in[3]) + (size_t)layer * 2048 * 6144 + (size_t)(kc * 128) * 6144 + nc * 256 + 4 * lane;
;         f32x4 acc[4];
; #pragma unroll
;         for (int b = 0; b < 4; ++b) acc[b] = (f32x4){0.f, 0.f, 0.f, 0.f};
; #pragma unroll 32
;         for (int k = 0; k < 128; ++k) { const f32x4 w = *(const f32x4*)(W + (size_t)k * 6144);
; #pragma unroll
;             for (int b = 0; b < 4; ++b) acc[b] += cond[b * 2048 + kc * 128 + k] * w; }
.LBB0_18:
	v_lshl_add_u64 v[76:77], v[138:139], 0, s[94:95]
	global_load_dwordx4 v[126:129], v[76:77], off nt
	v_mov_b32_e32 v124, s96
	ds_read_b128 v[140:143], v124
	ds_read_b128 v[64:67], v124 offset:16
	ds_read_b128 v[78:81], v124 offset:32
	s_movk_i32 s0, 0x6000
	v_add_co_u32_e64 v114, s[28:29], s0, v76
	ds_read_b128 v[144:147], v124 offset:8192
	ds_read_b128 v[50:53], v124 offset:8208
	ds_read_b128 v[148:151], v124 offset:16384
	ds_read_b128 v[46:49], v124 offset:16400
	ds_read_b128 v[152:155], v124 offset:24576
	ds_read_b128 v[42:45], v124 offset:24592
	ds_read_b128 v[56:59], v124 offset:48
	v_addc_co_u32_e64 v115, s[28:29], 0, v77, s[28:29]
	ds_read_b128 v[90:93], v124 offset:8224
	ds_read_b128 v[86:89], v124 offset:16416
	ds_read_b128 v[82:85], v124 offset:24608
	ds_read_b128 v[72:75], v124 offset:8240
	ds_read_b128 v[68:71], v124 offset:16432
	ds_read_b128 v[60:63], v124 offset:24624
	ds_read_b128 v[36:39], v124 offset:64
	ds_read_b128 v[32:35], v124 offset:8256
	ds_read_b128 v[28:31], v124 offset:16448
	ds_read_b128 v[24:27], v124 offset:24640
	ds_read_b128 v[4:7], v124 offset:80
	ds_read_b128 v[0:3], v124 offset:8272
	s_mov_b32 s0, 0xc000
	v_add_co_u32_e64 v130, s[26:27], s0, v76
	s_mov_b32 s0, 0x12000
	s_nop 0
	v_addc_co_u32_e64 v131, s[26:27], 0, v77, s[26:27]
	v_add_co_u32_e64 v156, s[36:37], s0, v76
	s_mov_b32 s0, 0x18000
	s_nop 0
	v_addc_co_u32_e64 v157, s[36:37], 0, v77, s[36:37]
	v_add_co_u32_e64 v158, s[42:43], s0, v76
	s_mov_b32 s0, 0x1e000
	s_nop 0
	v_addc_co_u32_e64 v159, s[42:43], 0, v77, s[42:43]
	v_add_co_u32_e64 v122, s[44:45], s0, v76
	s_mov_b32 s0, 0x24000
	s_nop 0
	v_addc_co_u32_e64 v123, s[44:45], 0, v77, s[44:45]
	v_add_co_u32_e64 v40, s[40:41], s0, v76
	s_mov_b32 s0, 0x2a000
	s_nop 0
	v_addc_co_u32_e64 v41, s[40:41], 0, v77, s[40:41]
	v_add_co_u32_e64 v120, s[24:25], s0, v76
	s_mov_b32 s0, 0x30000
	s_nop 0
	v_addc_co_u32_e64 v121, s[24:25], 0, v77, s[24:25]
	v_add_co_u32_e64 v54, s[22:23], s0, v76
	s_mov_b32 s0, 0x36000
	s_nop 0
	v_addc_co_u32_e64 v55, s[22:23], 0, v77, s[22:23]
	v_add_co_u32_e64 v118, s[20:21], s0, v76
	s_mov_b32 s33, 0x90000
	s_nop 0
	v_addc_co_u32_e64 v119, s[20:21], 0, v77, s[20:21]
	s_mov_b32 s0, 0x3c000
	v_add_co_u32_e32 v116, vcc, s0, v76
	s_mov_b32 s0, 0x42000
	s_mov_b32 s2, 0x48000
	s_mov_b32 s4, 0x4e000
	s_mov_b32 s6, 0x54000
	s_mov_b32 s8, 0x5a000
	s_mov_b32 s10, 0x60000
	s_mov_b32 s12, 0x66000
	s_mov_b32 s14, 0x6c000
	s_mov_b32 s16, 0x72000
	s_mov_b32 s18, 0x78000
	s_mov_b32 s26, 0x7e000
	s_mov_b32 s28, 0x84000
	s_mov_b32 s30, 0x8a000
	v_add_co_u32_e64 v98, s[0:1], s0, v76
	v_add_co_u32_e64 v96, s[2:3], s2, v76
	v_add_co_u32_e64 v112, s[4:5], s4, v76
	v_add_co_u32_e64 v108, s[6:7], s6, v76
	v_add_co_u32_e64 v102, s[8:9], s8, v76
	s_waitcnt vmcnt(0) lgkmcnt(14)
	v_pk_fma_f32 v[162:163], v[128:129], v[140:141], v[14:15] op_sel_hi:[1,0,1]
	v_pk_fma_f32 v[164:165], v[126:127], v[140:141], v[12:13] op_sel_hi:[1,0,1]
	global_load_dwordx4 v[12:15], v[114:115], off nt
	v_pk_fma_f32 v[18:19], v[128:129], v[144:145], v[18:19] op_sel_hi:[1,0,1]
	v_pk_fma_f32 v[16:17], v[126:127], v[144:145], v[16:17] op_sel_hi:[1,0,1]
	v_pk_fma_f32 v[22:23], v[128:129], v[148:149], v[22:23] op_sel_hi:[1,0,1]
	v_pk_fma_f32 v[20:21], v[126:127], v[148:149], v[20:21] op_sel_hi:[1,0,1]
	v_pk_fma_f32 v[128:129], v[128:129], v[152:153], v[10:11] op_sel_hi:[1,0,1]
	v_pk_fma_f32 v[126:127], v[126:127], v[152:153], v[8:9] op_sel_hi:[1,0,1]
	v_add_co_u32_e64 v100, s[10:11], s10, v76
	v_add_co_u32_e64 v110, s[12:13], s12, v76
	v_add_co_u32_e64 v104, s[14:15], s14, v76
	v_add_co_u32_e64 v106, s[16:17], s16, v76
	v_add_co_u32_e64 v94, s[18:19], s18, v76
	v_addc_co_u32_e32 v117, vcc, 0, v77, vcc
	v_addc_co_u32_e64 v99, vcc, 0, v77, s[0:1]
	v_addc_co_u32_e64 v97, vcc, 0, v77, s[2:3]
	v_addc_co_u32_e64 v113, vcc, 0, v77, s[4:5]
	v_addc_co_u32_e64 v109, vcc, 0, v77, s[6:7]
	v_addc_co_u32_e64 v103, vcc, 0, v77, s[8:9]
	v_addc_co_u32_e64 v101, vcc, 0, v77, s[10:11]
	v_addc_co_u32_e64 v111, vcc, 0, v77, s[12:13]
	v_addc_co_u32_e64 v105, vcc, 0, v77, s[14:15]
	v_addc_co_u32_e64 v107, vcc, 0, v77, s[16:17]
	v_addc_co_u32_e64 v95, vcc, 0, v77, s[18:19]
	ds_read_b128 v[8:11], v124 offset:16464
	s_waitcnt lgkmcnt(11)
	v_mov_b32_e32 v170, v89
	s_add_u32 s94, s94, 0xc0000
	s_addc_u32 s95, s95, 0
	s_addk_i32 s96, 0x80
	s_cmp_eq_u32 s94, 0x300000
	s_waitcnt vmcnt(0)
	v_pk_fma_f32 v[114:115], v[12:13], v[140:141], v[164:165] op_sel:[0,1,0]
	v_pk_fma_f32 v[140:141], v[14:15], v[140:141], v[162:163] op_sel:[0,1,0]
	v_pk_fma_f32 v[162:163], v[12:13], v[144:145], v[16:17] op_sel:[0,1,0]
	v_pk_fma_f32 v[144:145], v[14:15], v[144:145], v[18:19] op_sel:[0,1,0]
	global_load_dwordx4 v[16:19], v[130:131], off nt
	v_pk_fma_f32 v[126:127], v[12:13], v[152:153], v[126:127] op_sel:[0,1,0]
	v_pk_fma_f32 v[128:129], v[14:15], v[152:153], v[128:129] op_sel:[0,1,0]
	v_pk_fma_f32 v[20:21], v[12:13], v[148:149], v[20:21] op_sel:[0,1,0]
	v_pk_fma_f32 v[22:23], v[14:15], v[148:149], v[22:23] op_sel:[0,1,0]
	v_add_co_u32_e64 v148, s[28:29], s28, v76
	ds_read_b128 v[12:15], v124 offset:24656
	s_nop 0
	v_addc_co_u32_e64 v149, vcc, 0, v77, s[28:29]
	s_waitcnt vmcnt(0)
; __device__ __forceinline__ void p0a_mod_partials(Frame& F, const Args& A) {
;     ...
; #pragma unroll 32
;         for (int k = 0; k < 128; ++k) { const f32x4 w = *(const f32x4*)(W + (size_t)k * 6144);
; #pragma unroll
;             for (int b = 0; b < 4; ++b) acc[b] += cond[b * 2048 + kc * 128 + k] * w; }
	v_pk_fma_f32 v[164:165], v[18:19], v[154:155], v[128:129] op_sel_hi:[1,0,1]
	v_pk_fma_f32 v[166:167], v[16:17], v[154:155], v[126:127] op_sel_hi:[1,0,1]
	global_load_dwordx4 v[126:129], v[156:157], off nt
	v_pk_fma_f32 v[130:131], v[18:19], v[142:143], v[140:141] op_sel_hi:[1,0,1]
	v_pk_fma_f32 v[152:153], v[16:17], v[142:143], v[114:115] op_sel_hi:[1,0,1]
	v_pk_fma_f32 v[144:145], v[18:19], v[146:147], v[144:145] op_sel_hi:[1,0,1]
	v_pk_fma_f32 v[162:163], v[16:17], v[146:147], v[162:163] op_sel_hi:[1,0,1]
	v_pk_fma_f32 v[22:23], v[18:19], v[150:151], v[22:23] op_sel_hi:[1,0,1]
	v_pk_fma_f32 v[20:21], v[16:17], v[150:151], v[20:21] op_sel_hi:[1,0,1]
	v_mov_b32_e32 v16, v143
	v_mov_b32_e32 v142, v147
	v_mov_b32_e32 v150, v151
	v_mov_b32_e32 v154, v155
	v_add_co_u32_e64 v140, s[34:35], s33, v76
	s_mov_b32 s33, 0x96000
	v_add_co_u32_e64 v146, s[26:27], s26, v76
	v_add_co_u32_e64 v114, s[30:31], s30, v76
	s_nop 0
	v_addc_co_u32_e64 v147, vcc, 0, v77, s[26:27]
	v_addc_co_u32_e64 v115, vcc, 0, v77, s[30:31]
	v_addc_co_u32_e64 v141, vcc, 0, v77, s[34:35]
	s_waitcnt vmcnt(0)
	v_pk_fma_f32 v[130:131], v[128:129], v[16:17], v[130:131] op_sel_hi:[1,0,1]
	v_pk_fma_f32 v[152:153], v[126:127], v[16:17], v[152:153] op_sel_hi:[1,0,1]
	v_pk_fma_f32 v[156:157], v[128:129], v[142:143], v[144:145] op_sel_hi:[1,0,1]
	v_pk_fma_f32 v[162:163], v[126:127], v[142:143], v[162:163] op_sel_hi:[1,0,1]
	v_pk_fma_f32 v[168:169], v[128:129], v[150:151], v[22:23] op_sel_hi:[1,0,1]
	v_pk_fma_f32 v[150:151], v[126:127], v[150:151], v[20:21] op_sel_hi:[1,0,1]
	v_pk_fma_f32 v[164:165], v[128:129], v[154:155], v[164:165] op_sel_hi:[1,0,1]
	v_pk_fma_f32 v[154:155], v[126:127], v[154:155], v[166:167] op_sel_hi:[1,0,1]
	global_load_dwordx4 v[126:129], v[158:159], off nt
	v_add_co_u32_e64 v142, s[36:37], s33, v76
	s_mov_b32 s33, 0x9c000
	v_add_co_u32_e64 v144, s[38:39], s33, v76
	s_mov_b32 s33, 0xa2000
	v_addc_co_u32_e64 v143, vcc, 0, v77, s[36:37]
	v_addc_co_u32_e64 v145, vcc, 0, v77, s[38:39]
	ds_read_b128 v[16:19], v124 offset:96
	ds_read_b128 v[20:23], v124 offset:8288
	s_waitcnt vmcnt(0)
	v_pk_fma_f32 v[130:131], v[128:129], v[64:65], v[130:131] op_sel_hi:[1,0,1]
	v_pk_fma_f32 v[152:153], v[126:127], v[64:65], v[152:153] op_sel_hi:[1,0,1]
	v_pk_fma_f32 v[156:157], v[128:129], v[50:51], v[156:157] op_sel_hi:[1,0,1]
	v_pk_fma_f32 v[158:159], v[126:127], v[50:51], v[162:163] op_sel_hi:[1,0,1]
	v_pk_fma_f32 v[162:163], v[128:129], v[46:47], v[168:169] op_sel_hi:[1,0,1]
	v_pk_fma_f32 v[166:167], v[126:127], v[46:47], v[150:151] op_sel_hi:[1,0,1]
	v_pk_fma_f32 v[164:165], v[128:129], v[42:43], v[164:165] op_sel_hi:[1,0,1]
	v_pk_fma_f32 v[154:155], v[126:127], v[42:43], v[154:155] op_sel_hi:[1,0,1]
	global_load_dwordx4 v[126:129], v[122:123], off nt
	v_mov_b32_e32 v168, v49
	v_add_co_u32_e64 v150, s[42:43], s33, v76
	s_mov_b32 s33, 0xa8000
	s_nop 0
	v_addc_co_u32_e64 v151, vcc, 0, v77, s[42:43]
	s_waitcnt vmcnt(0)
	v_pk_fma_f32 v[122:123], v[128:129], v[64:65], v[130:131] op_sel:[0,1,0]
	v_pk_fma_f32 v[64:65], v[126:127], v[64:65], v[152:153] op_sel:[0,1,0]
	v_pk_fma_f32 v[130:131], v[128:129], v[50:51], v[156:157] op_sel:[0,1,0]
	v_pk_fma_f32 v[50:51], v[126:127], v[50:51], v[158:159] op_sel:[0,1,0]
	v_pk_fma_f32 v[156:157], v[128:129], v[46:47], v[162:163] op_sel:[0,1,0]
	v_pk_fma_f32 v[46:47], v[126:127], v[46:47], v[166:167] op_sel:[0,1,0]
	v_pk_fma_f32 v[128:129], v[128:129], v[42:43], v[164:165] op_sel:[0,1,0]
	v_pk_fma_f32 v[126:127], v[126:127], v[42:43], v[154:155] op_sel:[0,1,0]
	global_load_dwordx4 v[40:43], v[40:41], off nt
	v_add_co_u32_e64 v152, s[44:45], s33, v76
	s_mov_b32 s33, 0xae000
	v_add_co_u32_e64 v154, s[40:41], s33, v76
	s_mov_b32 s33, 0xb4000
	v_add_co_u32_e64 v158, s[46:47], s33, v76
	s_mov_b32 s33, 0xba000
	v_addc_co_u32_e64 v153, vcc, 0, v77, s[44:45]
	v_addc_co_u32_e64 v155, vcc, 0, v77, s[40:41]
	v_addc_co_u32_e64 v159, vcc, 0, v77, s[46:47]
	s_waitcnt vmcnt(0)
	v_pk_fma_f32 v[162:163], v[40:41], v[52:53], v[50:51] op_sel_hi:[1,0,1]
	v_pk_fma_f32 v[164:165], v[42:43], v[48:49], v[156:157] op_sel_hi:[1,0,1]
	v_pk_fma_f32 v[166:167], v[40:41], v[48:49], v[46:47] op_sel_hi:[1,0,1]
	global_load_dwordx4 v[48:51], v[120:121], off nt
	v_pk_fma_f32 v[122:123], v[42:43], v[66:67], v[122:123] op_sel_hi:[1,0,1]
	v_pk_fma_f32 v[64:65], v[40:41], v[66:67], v[64:65] op_sel_hi:[1,0,1]
	v_mov_b32_e32 v66, v67
	v_pk_fma_f32 v[130:131], v[42:43], v[52:53], v[130:131] op_sel_hi:[1,0,1]
	v_mov_b32_e32 v52, v53
	v_add_co_u32_e64 v156, s[48:49], s33, v76
	v_pk_fma_f32 v[128:129], v[42:43], v[44:45], v[128:129] op_sel_hi:[1,0,1]
	v_pk_fma_f32 v[126:127], v[40:41], v[44:45], v[126:127] op_sel_hi:[1,0,1]
	v_mov_b32_e32 v76, v45
	v_addc_co_u32_e64 v157, vcc, 0, v77, s[48:49]
	ds_read_b128 v[40:43], v124 offset:16480
	ds_read_b128 v[44:47], v124 offset:112
	s_waitcnt vmcnt(0)
	v_pk_fma_f32 v[120:121], v[50:51], v[66:67], v[122:123] op_sel_hi:[1,0,1]
	v_pk_fma_f32 v[64:65], v[48:49], v[66:67], v[64:65] op_sel_hi:[1,0,1]
	v_pk_fma_f32 v[66:67], v[50:51], v[52:53], v[130:131] op_sel_hi:[1,0,1]
	v_pk_fma_f32 v[122:123], v[48:49], v[52:53], v[162:163] op_sel_hi:[1,0,1]
	global_load_dwordx4 v[52:55], v[54:55], off nt
	v_pk_fma_f32 v[130:131], v[50:51], v[168:169], v[164:165] op_sel_hi:[1,0,1]
	v_pk_fma_f32 v[162:163], v[48:49], v[168:169], v[166:167] op_sel_hi:[1,0,1]
	v_pk_fma_f32 v[128:129], v[50:51], v[76:77], v[128:129] op_sel_hi:[1,0,1]
	v_pk_fma_f32 v[126:127], v[48:49], v[76:77], v[126:127] op_sel_hi:[1,0,1]
	ds_read_b128 v[48:51], v124 offset:8304
	s_waitcnt vmcnt(0)
; __device__ __forceinline__ void p0a_mod_partials(Frame& F, const Args& A) {
;     ...
; #pragma unroll 32
;         for (int k = 0; k < 128; ++k) { const f32x4 w = *(const f32x4*)(W + (size_t)k * 6144);
; #pragma unroll
;             for (int b = 0; b < 4; ++b) acc[b] += cond[b * 2048 + kc * 128 + k] * w; }
	v_pk_fma_f32 v[164:165], v[52:53], v[78:79], v[64:65] op_sel_hi:[1,0,1]
	v_pk_fma_f32 v[166:167], v[54:55], v[90:91], v[66:67] op_sel_hi:[1,0,1]
	global_load_dwordx4 v[64:67], v[118:119], off nt
	v_pk_fma_f32 v[120:121], v[54:55], v[78:79], v[120:121] op_sel_hi:[1,0,1]
	s_waitcnt lgkmcnt(14)
	v_pk_fma_f32 v[128:129], v[54:55], v[82:83], v[128:129] op_sel_hi:[1,0,1]
	v_pk_fma_f32 v[126:127], v[52:53], v[82:83], v[126:127] op_sel_hi:[1,0,1]
	v_pk_fma_f32 v[122:123], v[52:53], v[90:91], v[122:123] op_sel_hi:[1,0,1]
	v_pk_fma_f32 v[130:131], v[54:55], v[86:87], v[130:131] op_sel_hi:[1,0,1]
	v_pk_fma_f32 v[162:163], v[52:53], v[86:87], v[162:163] op_sel_hi:[1,0,1]
	ds_read_b128 v[52:55], v124 offset:16496
	s_waitcnt vmcnt(0)
	v_pk_fma_f32 v[118:119], v[66:67], v[78:79], v[120:121] op_sel:[0,1,0]
	v_pk_fma_f32 v[120:121], v[64:65], v[78:79], v[164:165] op_sel:[0,1,0]
	global_load_dwordx4 v[76:79], v[116:117], off nt
	v_pk_fma_f32 v[128:129], v[66:67], v[82:83], v[128:129] op_sel:[0,1,0]
	v_pk_fma_f32 v[82:83], v[64:65], v[82:83], v[126:127] op_sel:[0,1,0]
	v_pk_fma_f32 v[164:165], v[66:67], v[90:91], v[166:167] op_sel:[0,1,0]
	v_pk_fma_f32 v[90:91], v[64:65], v[90:91], v[122:123] op_sel:[0,1,0]
	v_pk_fma_f32 v[122:123], v[66:67], v[86:87], v[130:131] op_sel:[0,1,0]
	v_pk_fma_f32 v[86:87], v[64:65], v[86:87], v[162:163] op_sel:[0,1,0]
	ds_read_b128 v[64:67], v124 offset:24672
	s_waitcnt vmcnt(0)
	v_pk_fma_f32 v[116:117], v[78:79], v[80:81], v[118:119] op_sel_hi:[1,0,1]
	v_pk_fma_f32 v[118:119], v[76:77], v[80:81], v[120:121] op_sel_hi:[1,0,1]
	v_pk_fma_f32 v[166:167], v[78:79], v[84:85], v[128:129] op_sel_hi:[1,0,1]
	v_pk_fma_f32 v[168:169], v[76:77], v[84:85], v[82:83] op_sel_hi:[1,0,1]
	v_mov_b32_e32 v84, v81
	global_load_dwordx4 v[80:83], v[98:99], off nt
	v_pk_fma_f32 v[120:121], v[78:79], v[92:93], v[164:165] op_sel_hi:[1,0,1]
	v_pk_fma_f32 v[126:127], v[76:77], v[92:93], v[90:91] op_sel_hi:[1,0,1]
	v_pk_fma_f32 v[122:123], v[78:79], v[88:89], v[122:123] op_sel_hi:[1,0,1]
	v_pk_fma_f32 v[86:87], v[76:77], v[88:89], v[86:87] op_sel_hi:[1,0,1]
	v_mov_b32_e32 v88, v93
	global_load_dwordx4 v[90:93], v[96:97], off nt
	global_load_dwordx4 v[162:165], v[108:109], off nt
	global_load_dwordx4 v[128:131], v[102:103], off nt
	ds_read_b128 v[76:79], v124 offset:24688
	global_load_dwordx4 v[96:99], v[112:113], off nt
	v_mov_b32_e32 v112, v85
	s_waitcnt vmcnt(4)
	v_pk_fma_f32 v[102:103], v[82:83], v[88:89], v[120:121] op_sel_hi:[1,0,1]
	v_pk_fma_f32 v[88:89], v[80:81], v[88:89], v[126:127] op_sel_hi:[1,0,1]
	global_load_dwordx4 v[124:127], v[100:101], off nt
	v_pk_fma_f32 v[100:101], v[82:83], v[170:171], v[122:123] op_sel_hi:[1,0,1]
	global_load_dwordx4 v[120:123], v[110:111], off nt
	v_pk_fma_f32 v[108:109], v[82:83], v[84:85], v[116:117] op_sel_hi:[1,0,1]
	v_pk_fma_f32 v[172:173], v[80:81], v[84:85], v[118:119] op_sel_hi:[1,0,1]
	v_pk_fma_f32 v[170:171], v[80:81], v[170:171], v[86:87] op_sel_hi:[1,0,1]
	v_pk_fma_f32 v[110:111], v[82:83], v[112:113], v[166:167] op_sel_hi:[1,0,1]
	v_pk_fma_f32 v[112:113], v[80:81], v[112:113], v[168:169] op_sel_hi:[1,0,1]
	global_load_dwordx4 v[116:119], v[104:105], off nt
	global_load_dwordx4 v[80:83], v[106:107], off nt
	global_load_dwordx4 v[84:87], v[94:95], off nt
	s_waitcnt vmcnt(8)
	v_pk_fma_f32 v[104:105], v[92:93], v[56:57], v[108:109] op_sel_hi:[1,0,1]
	v_pk_fma_f32 v[106:107], v[90:91], v[56:57], v[172:173] op_sel_hi:[1,0,1]
	v_pk_fma_f32 v[102:103], v[92:93], v[72:73], v[102:103] op_sel_hi:[1,0,1]
	v_pk_fma_f32 v[108:109], v[90:91], v[72:73], v[88:89] op_sel_hi:[1,0,1]
	v_pk_fma_f32 v[100:101], v[92:93], v[68:69], v[100:101] op_sel_hi:[1,0,1]
	v_pk_fma_f32 v[166:167], v[90:91], v[68:69], v[170:171] op_sel_hi:[1,0,1]
	s_waitcnt lgkmcnt(14)
	v_pk_fma_f32 v[110:111], v[92:93], v[60:61], v[110:111] op_sel_hi:[1,0,1]
	v_pk_fma_f32 v[112:113], v[90:91], v[60:61], v[112:113] op_sel_hi:[1,0,1]
	global_load_dwordx4 v[92:95], v[146:147], off nt
	global_load_dwordx4 v[88:91], v[148:149], off nt
	s_waitcnt vmcnt(7)
	v_pk_fma_f32 v[104:105], v[98:99], v[56:57], v[104:105] op_sel:[0,1,0]
	v_pk_fma_f32 v[56:57], v[96:97], v[56:57], v[106:107] op_sel:[0,1,0]
	v_pk_fma_f32 v[106:107], v[98:99], v[72:73], v[102:103] op_sel:[0,1,0]
	v_pk_fma_f32 v[72:73], v[96:97], v[72:73], v[108:109] op_sel:[0,1,0]
	v_pk_fma_f32 v[108:109], v[98:99], v[68:69], v[100:101] op_sel:[0,1,0]
	v_pk_fma_f32 v[68:69], v[96:97], v[68:69], v[166:167] op_sel:[0,1,0]
	v_pk_fma_f32 v[110:111], v[98:99], v[60:61], v[110:111] op_sel:[0,1,0]
	v_pk_fma_f32 v[60:61], v[96:97], v[60:61], v[112:113] op_sel:[0,1,0]
	global_load_dwordx4 v[100:103], v[114:115], off nt
	global_load_dwordx4 v[96:99], v[140:141], off nt
	v_pk_fma_f32 v[140:141], v[164:165], v[58:59], v[104:105] op_sel_hi:[1,0,1]
	v_pk_fma_f32 v[148:149], v[164:165], v[74:75], v[106:107] op_sel_hi:[1,0,1]
	v_pk_fma_f32 v[168:169], v[164:165], v[70:71], v[108:109] op_sel_hi:[1,0,1]
	v_pk_fma_f32 v[164:165], v[164:165], v[62:63], v[110:111] op_sel_hi:[1,0,1]
	global_load_dwordx4 v[112:115], v[142:143], off nt
	global_load_dwordx4 v[108:111], v[144:145], off nt
	global_load_dwordx4 v[104:107], v[150:151], off nt
	v_pk_fma_f32 v[166:167], v[162:163], v[74:75], v[72:73] op_sel_hi:[1,0,1]
	v_mov_b32_e32 v142, v75
	global_load_dwordx4 v[72:75], v[152:153], off nt
	v_pk_fma_f32 v[170:171], v[162:163], v[70:71], v[68:69] op_sel_hi:[1,0,1]
	v_mov_b32_e32 v144, v71
	global_load_dwordx4 v[68:71], v[154:155], off nt
	v_pk_fma_f32 v[146:147], v[162:163], v[58:59], v[56:57] op_sel_hi:[1,0,1]
	v_pk_fma_f32 v[162:163], v[162:163], v[62:63], v[60:61] op_sel_hi:[1,0,1]
	v_mov_b32_e32 v60, v59
	global_load_dwordx4 v[56:59], v[158:159], off nt
	v_mov_b32_e32 v150, v63
	v_pk_fma_f32 v[152:153], v[130:131], v[60:61], v[140:141] op_sel_hi:[1,0,1]
	v_pk_fma_f32 v[146:147], v[128:129], v[60:61], v[146:147] op_sel_hi:[1,0,1]
	global_load_dwordx4 v[60:63], v[156:157], off nt
	v_pk_fma_f32 v[148:149], v[130:131], v[142:143], v[148:149] op_sel_hi:[1,0,1]
	v_pk_fma_f32 v[154:155], v[128:129], v[142:143], v[166:167] op_sel_hi:[1,0,1]
	v_pk_fma_f32 v[156:157], v[130:131], v[144:145], v[168:169] op_sel_hi:[1,0,1]
	v_pk_fma_f32 v[158:159], v[128:129], v[144:145], v[170:171] op_sel_hi:[1,0,1]
	v_pk_fma_f32 v[164:165], v[130:131], v[150:151], v[164:165] op_sel_hi:[1,0,1]
	v_pk_fma_f32 v[150:151], v[128:129], v[150:151], v[162:163] op_sel_hi:[1,0,1]
	v_mov_b32_e32 v140, v39
	v_mov_b32_e32 v142, v35
	s_waitcnt lgkmcnt(13)
; __device__ __forceinline__ void p0a_mod_partials(Frame& F, const Args& A) {
;     ...
; #pragma unroll 32
;         for (int k = 0; k < 128; ++k) { const f32x4 w = *(const f32x4*)(W + (size_t)k * 6144);
; #pragma unroll
;             for (int b = 0; b < 4; ++b) acc[b] += cond[b * 2048 + kc * 128 + k] * w; }
	v_mov_b32_e32 v130, v31
	s_waitcnt lgkmcnt(12)
	v_mov_b32_e32 v144, v27
	s_waitcnt lgkmcnt(11)
	v_mov_b32_e32 v128, v7
	s_waitcnt vmcnt(15)
	v_pk_fma_f32 v[152:153], v[126:127], v[36:37], v[152:153] op_sel_hi:[1,0,1]
	v_pk_fma_f32 v[146:147], v[124:125], v[36:37], v[146:147] op_sel_hi:[1,0,1]
	v_pk_fma_f32 v[148:149], v[126:127], v[32:33], v[148:149] op_sel_hi:[1,0,1]
	v_pk_fma_f32 v[154:155], v[124:125], v[32:33], v[154:155] op_sel_hi:[1,0,1]
	v_pk_fma_f32 v[156:157], v[126:127], v[28:29], v[156:157] op_sel_hi:[1,0,1]
	v_pk_fma_f32 v[158:159], v[124:125], v[28:29], v[158:159] op_sel_hi:[1,0,1]
	v_pk_fma_f32 v[162:163], v[126:127], v[24:25], v[164:165] op_sel_hi:[1,0,1]
	v_pk_fma_f32 v[150:151], v[124:125], v[24:25], v[150:151] op_sel_hi:[1,0,1]
	s_waitcnt vmcnt(14)
	v_pk_fma_f32 v[152:153], v[122:123], v[36:37], v[152:153] op_sel:[0,1,0]
	v_pk_fma_f32 v[36:37], v[120:121], v[36:37], v[146:147] op_sel:[0,1,0]
	v_pk_fma_f32 v[146:147], v[122:123], v[32:33], v[148:149] op_sel:[0,1,0]
	v_pk_fma_f32 v[148:149], v[120:121], v[32:33], v[154:155] op_sel:[0,1,0]
	v_pk_fma_f32 v[154:155], v[122:123], v[28:29], v[156:157] op_sel:[0,1,0]
	v_pk_fma_f32 v[156:157], v[120:121], v[28:29], v[158:159] op_sel:[0,1,0]
	v_pk_fma_f32 v[122:123], v[122:123], v[24:25], v[162:163] op_sel:[0,1,0]
	v_pk_fma_f32 v[150:151], v[120:121], v[24:25], v[150:151] op_sel:[0,1,0]
	s_waitcnt vmcnt(13)
	v_pk_fma_f32 v[152:153], v[118:119], v[38:39], v[152:153] op_sel_hi:[1,0,1]
	v_pk_fma_f32 v[158:159], v[116:117], v[38:39], v[36:37] op_sel_hi:[1,0,1]
	v_pk_fma_f32 v[146:147], v[118:119], v[34:35], v[146:147] op_sel_hi:[1,0,1]
	v_pk_fma_f32 v[148:149], v[116:117], v[34:35], v[148:149] op_sel_hi:[1,0,1]
	v_pk_fma_f32 v[154:155], v[118:119], v[30:31], v[154:155] op_sel_hi:[1,0,1]
	v_pk_fma_f32 v[156:157], v[116:117], v[30:31], v[156:157] op_sel_hi:[1,0,1]
	v_pk_fma_f32 v[118:119], v[118:119], v[26:27], v[122:123] op_sel_hi:[1,0,1]
	v_pk_fma_f32 v[26:27], v[116:117], v[26:27], v[150:151] op_sel_hi:[1,0,1]
	s_waitcnt vmcnt(12)
	v_pk_fma_f32 v[122:123], v[82:83], v[140:141], v[152:153] op_sel_hi:[1,0,1]
	v_pk_fma_f32 v[140:141], v[80:81], v[140:141], v[158:159] op_sel_hi:[1,0,1]
	v_pk_fma_f32 v[146:147], v[82:83], v[142:143], v[146:147] op_sel_hi:[1,0,1]
	v_pk_fma_f32 v[142:143], v[80:81], v[142:143], v[148:149] op_sel_hi:[1,0,1]
	v_pk_fma_f32 v[148:149], v[82:83], v[130:131], v[154:155] op_sel_hi:[1,0,1]
	v_pk_fma_f32 v[130:131], v[80:81], v[130:131], v[156:157] op_sel_hi:[1,0,1]
	v_pk_fma_f32 v[82:83], v[82:83], v[144:145], v[118:119] op_sel_hi:[1,0,1]
	v_pk_fma_f32 v[26:27], v[80:81], v[144:145], v[26:27] op_sel_hi:[1,0,1]
	s_waitcnt vmcnt(11)
	v_pk_fma_f32 v[80:81], v[86:87], v[4:5], v[122:123] op_sel_hi:[1,0,1]
	v_pk_fma_f32 v[118:119], v[84:85], v[4:5], v[140:141] op_sel_hi:[1,0,1]
	s_waitcnt lgkmcnt(10)
	v_pk_fma_f32 v[122:123], v[86:87], v[0:1], v[146:147] op_sel_hi:[1,0,1]
	v_pk_fma_f32 v[140:141], v[84:85], v[0:1], v[142:143] op_sel_hi:[1,0,1]
	s_waitcnt lgkmcnt(9)
	v_pk_fma_f32 v[142:143], v[86:87], v[8:9], v[148:149] op_sel_hi:[1,0,1]
	v_pk_fma_f32 v[130:131], v[84:85], v[8:9], v[130:131] op_sel_hi:[1,0,1]
	s_waitcnt lgkmcnt(8)
	v_pk_fma_f32 v[82:83], v[86:87], v[12:13], v[82:83] op_sel_hi:[1,0,1]
	v_pk_fma_f32 v[26:27], v[84:85], v[12:13], v[26:27] op_sel_hi:[1,0,1]
	s_waitcnt vmcnt(10)
	v_pk_fma_f32 v[80:81], v[94:95], v[4:5], v[80:81] op_sel:[0,1,0]
	v_pk_fma_f32 v[4:5], v[92:93], v[4:5], v[118:119] op_sel:[0,1,0]
	v_pk_fma_f32 v[84:85], v[94:95], v[0:1], v[122:123] op_sel:[0,1,0]
	v_pk_fma_f32 v[0:1], v[92:93], v[0:1], v[140:141] op_sel:[0,1,0]
	v_pk_fma_f32 v[86:87], v[94:95], v[8:9], v[142:143] op_sel:[0,1,0]
	v_pk_fma_f32 v[8:9], v[92:93], v[8:9], v[130:131] op_sel:[0,1,0]
	v_pk_fma_f32 v[82:83], v[94:95], v[12:13], v[82:83] op_sel:[0,1,0]
	v_pk_fma_f32 v[12:13], v[92:93], v[12:13], v[26:27] op_sel:[0,1,0]
	v_mov_b32_e32 v126, v3
	v_mov_b32_e32 v124, v11
	v_mov_b32_e32 v120, v15
	s_waitcnt vmcnt(9)
	v_pk_fma_f32 v[26:27], v[90:91], v[6:7], v[80:81] op_sel_hi:[1,0,1]
	v_pk_fma_f32 v[4:5], v[88:89], v[6:7], v[4:5] op_sel_hi:[1,0,1]
	v_pk_fma_f32 v[6:7], v[90:91], v[2:3], v[84:85] op_sel_hi:[1,0,1]
	v_pk_fma_f32 v[0:1], v[88:89], v[2:3], v[0:1] op_sel_hi:[1,0,1]
	v_pk_fma_f32 v[2:3], v[90:91], v[10:11], v[86:87] op_sel_hi:[1,0,1]
	v_pk_fma_f32 v[8:9], v[88:89], v[10:11], v[8:9] op_sel_hi:[1,0,1]
	v_pk_fma_f32 v[10:11], v[90:91], v[14:15], v[82:83] op_sel_hi:[1,0,1]
	v_pk_fma_f32 v[12:13], v[88:89], v[14:15], v[12:13] op_sel_hi:[1,0,1]
	s_waitcnt vmcnt(8)
	v_pk_fma_f32 v[14:15], v[102:103], v[128:129], v[26:27] op_sel_hi:[1,0,1]
	v_pk_fma_f32 v[4:5], v[100:101], v[128:129], v[4:5] op_sel_hi:[1,0,1]
	v_pk_fma_f32 v[6:7], v[102:103], v[126:127], v[6:7] op_sel_hi:[1,0,1]
	v_pk_fma_f32 v[0:1], v[100:101], v[126:127], v[0:1] op_sel_hi:[1,0,1]
	v_pk_fma_f32 v[2:3], v[102:103], v[124:125], v[2:3] op_sel_hi:[1,0,1]
	v_pk_fma_f32 v[8:9], v[100:101], v[124:125], v[8:9] op_sel_hi:[1,0,1]
	v_pk_fma_f32 v[10:11], v[102:103], v[120:121], v[10:11] op_sel_hi:[1,0,1]
	v_pk_fma_f32 v[12:13], v[100:101], v[120:121], v[12:13] op_sel_hi:[1,0,1]
	s_waitcnt vmcnt(7) lgkmcnt(7)
	v_pk_fma_f32 v[14:15], v[98:99], v[16:17], v[14:15] op_sel_hi:[1,0,1]
	v_pk_fma_f32 v[4:5], v[96:97], v[16:17], v[4:5] op_sel_hi:[1,0,1]
	s_waitcnt lgkmcnt(6)
; __device__ __forceinline__ void p0a_mod_partials(Frame& F, const Args& A) {
;     ...
;     for (int u = gw; u < 1536; u += NGW) {
;         const int j = u / 384, r = u % 384, nc = r / 16, kc = r % 16, layer = j >> 1;
;         const float* W = ((j & 1) ? A.in[6] : A.in[3]) + (size_t)layer * 2048 * 6144 + (size_t)(kc * 128) * 6144 + nc * 256 + 4 * lane;
;         f32x4 acc[4];
; #pragma unroll
;         for (int b = 0; b < 4; ++b) acc[b] = (f32x4){0.f, 0.f, 0.f, 0.f};
; #pragma unroll 32
;         for (int k = 0; k < 128; ++k) { const f32x4 w = *(const f32x4*)(W + (size_t)k * 6144);
; #pragma unroll
;             for (int b = 0; b < 4; ++b) acc[b] += cond[b * 2048 + kc * 128 + k] * w; }
; #pragma unroll
;         for (int b = 0; b < 4; ++b) *(f32x4*)(MODP + ((size_t)(kc * 16 + j * 4 + b)) * 6144 + nc * 256 + 4 * lane) = acc[b];
	v_pk_fma_f32 v[6:7], v[98:99], v[20:21], v[6:7] op_sel_hi:[1,0,1]
	v_pk_fma_f32 v[0:1], v[96:97], v[20:21], v[0:1] op_sel_hi:[1,0,1]
	s_waitcnt lgkmcnt(5)
	v_pk_fma_f32 v[2:3], v[98:99], v[40:41], v[2:3] op_sel_hi:[1,0,1]
	v_pk_fma_f32 v[8:9], v[96:97], v[40:41], v[8:9] op_sel_hi:[1,0,1]
	s_waitcnt lgkmcnt(1)
	v_pk_fma_f32 v[10:11], v[98:99], v[64:65], v[10:11] op_sel_hi:[1,0,1]
	v_pk_fma_f32 v[12:13], v[96:97], v[64:65], v[12:13] op_sel_hi:[1,0,1]
	s_waitcnt vmcnt(6)
	v_pk_fma_f32 v[14:15], v[114:115], v[16:17], v[14:15] op_sel:[0,1,0]
	v_pk_fma_f32 v[4:5], v[112:113], v[16:17], v[4:5] op_sel:[0,1,0]
	v_pk_fma_f32 v[6:7], v[114:115], v[20:21], v[6:7] op_sel:[0,1,0]
	v_pk_fma_f32 v[0:1], v[112:113], v[20:21], v[0:1] op_sel:[0,1,0]
	v_pk_fma_f32 v[2:3], v[114:115], v[40:41], v[2:3] op_sel:[0,1,0]
	v_pk_fma_f32 v[8:9], v[112:113], v[40:41], v[8:9] op_sel:[0,1,0]
	v_pk_fma_f32 v[10:11], v[114:115], v[64:65], v[10:11] op_sel:[0,1,0]
	v_pk_fma_f32 v[12:13], v[112:113], v[64:65], v[12:13] op_sel:[0,1,0]
	v_mov_b32_e32 v28, v19
	v_mov_b32_e32 v32, v23
	v_mov_b32_e32 v36, v43
	v_mov_b32_e32 v38, v67
	s_waitcnt vmcnt(5)
	v_pk_fma_f32 v[14:15], v[110:111], v[18:19], v[14:15] op_sel_hi:[1,0,1]
	v_pk_fma_f32 v[4:5], v[108:109], v[18:19], v[4:5] op_sel_hi:[1,0,1]
	v_pk_fma_f32 v[6:7], v[110:111], v[22:23], v[6:7] op_sel_hi:[1,0,1]
	v_pk_fma_f32 v[0:1], v[108:109], v[22:23], v[0:1] op_sel_hi:[1,0,1]
	v_pk_fma_f32 v[2:3], v[110:111], v[42:43], v[2:3] op_sel_hi:[1,0,1]
	v_pk_fma_f32 v[8:9], v[108:109], v[42:43], v[8:9] op_sel_hi:[1,0,1]
	v_pk_fma_f32 v[10:11], v[110:111], v[66:67], v[10:11] op_sel_hi:[1,0,1]
	v_pk_fma_f32 v[12:13], v[108:109], v[66:67], v[12:13] op_sel_hi:[1,0,1]
	s_waitcnt vmcnt(4)
	v_pk_fma_f32 v[14:15], v[106:107], v[28:29], v[14:15] op_sel_hi:[1,0,1]
	v_pk_fma_f32 v[4:5], v[104:105], v[28:29], v[4:5] op_sel_hi:[1,0,1]
	v_pk_fma_f32 v[6:7], v[106:107], v[32:33], v[6:7] op_sel_hi:[1,0,1]
	v_pk_fma_f32 v[0:1], v[104:105], v[32:33], v[0:1] op_sel_hi:[1,0,1]
	v_pk_fma_f32 v[2:3], v[106:107], v[36:37], v[2:3] op_sel_hi:[1,0,1]
	v_pk_fma_f32 v[8:9], v[104:105], v[36:37], v[8:9] op_sel_hi:[1,0,1]
	v_pk_fma_f32 v[10:11], v[106:107], v[38:39], v[10:11] op_sel_hi:[1,0,1]
	v_pk_fma_f32 v[12:13], v[104:105], v[38:39], v[12:13] op_sel_hi:[1,0,1]
	s_waitcnt vmcnt(3)
	v_pk_fma_f32 v[14:15], v[74:75], v[44:45], v[14:15] op_sel_hi:[1,0,1]
	v_pk_fma_f32 v[4:5], v[72:73], v[44:45], v[4:5] op_sel_hi:[1,0,1]
	v_pk_fma_f32 v[6:7], v[74:75], v[48:49], v[6:7] op_sel_hi:[1,0,1]
	v_pk_fma_f32 v[0:1], v[72:73], v[48:49], v[0:1] op_sel_hi:[1,0,1]
	v_pk_fma_f32 v[2:3], v[74:75], v[52:53], v[2:3] op_sel_hi:[1,0,1]
	v_pk_fma_f32 v[8:9], v[72:73], v[52:53], v[8:9] op_sel_hi:[1,0,1]
	s_waitcnt lgkmcnt(0)
	v_pk_fma_f32 v[10:11], v[74:75], v[76:77], v[10:11] op_sel_hi:[1,0,1]
	v_pk_fma_f32 v[12:13], v[72:73], v[76:77], v[12:13] op_sel_hi:[1,0,1]
	s_waitcnt vmcnt(2)
	v_pk_fma_f32 v[14:15], v[70:71], v[44:45], v[14:15] op_sel:[0,1,0]
	v_pk_fma_f32 v[4:5], v[68:69], v[44:45], v[4:5] op_sel:[0,1,0]
	v_pk_fma_f32 v[6:7], v[70:71], v[48:49], v[6:7] op_sel:[0,1,0]
	v_pk_fma_f32 v[0:1], v[68:69], v[48:49], v[0:1] op_sel:[0,1,0]
	v_pk_fma_f32 v[2:3], v[70:71], v[52:53], v[2:3] op_sel:[0,1,0]
	v_pk_fma_f32 v[8:9], v[68:69], v[52:53], v[8:9] op_sel:[0,1,0]
	v_pk_fma_f32 v[10:11], v[70:71], v[76:77], v[10:11] op_sel:[0,1,0]
	v_pk_fma_f32 v[12:13], v[68:69], v[76:77], v[12:13] op_sel:[0,1,0]
	v_mov_b32_e32 v24, v47
	v_mov_b32_e32 v34, v51
	v_mov_b32_e32 v30, v55
	v_mov_b32_e32 v116, v79
	s_waitcnt vmcnt(1)
	v_pk_fma_f32 v[14:15], v[58:59], v[46:47], v[14:15] op_sel_hi:[1,0,1]
	v_pk_fma_f32 v[4:5], v[56:57], v[46:47], v[4:5] op_sel_hi:[1,0,1]
	v_pk_fma_f32 v[6:7], v[58:59], v[50:51], v[6:7] op_sel_hi:[1,0,1]
	v_pk_fma_f32 v[0:1], v[56:57], v[50:51], v[0:1] op_sel_hi:[1,0,1]
	v_pk_fma_f32 v[2:3], v[58:59], v[54:55], v[2:3] op_sel_hi:[1,0,1]
	v_pk_fma_f32 v[8:9], v[56:57], v[54:55], v[8:9] op_sel_hi:[1,0,1]
	v_pk_fma_f32 v[10:11], v[58:59], v[78:79], v[10:11] op_sel_hi:[1,0,1]
	v_pk_fma_f32 v[26:27], v[56:57], v[78:79], v[12:13] op_sel_hi:[1,0,1]
	s_waitcnt vmcnt(0)
	v_pk_fma_f32 v[14:15], v[62:63], v[24:25], v[14:15] op_sel_hi:[1,0,1]
	v_pk_fma_f32 v[12:13], v[60:61], v[24:25], v[4:5] op_sel_hi:[1,0,1]
	v_pk_fma_f32 v[18:19], v[62:63], v[34:35], v[6:7] op_sel_hi:[1,0,1]
	v_pk_fma_f32 v[16:17], v[60:61], v[34:35], v[0:1] op_sel_hi:[1,0,1]
	v_pk_fma_f32 v[22:23], v[62:63], v[30:31], v[2:3] op_sel_hi:[1,0,1]
	v_pk_fma_f32 v[20:21], v[60:61], v[30:31], v[8:9] op_sel_hi:[1,0,1]
	v_pk_fma_f32 v[10:11], v[62:63], v[116:117], v[10:11] op_sel_hi:[1,0,1]
	v_pk_fma_f32 v[8:9], v[60:61], v[116:117], v[26:27] op_sel_hi:[1,0,1]
	s_cbranch_scc0 .LBB0_18
	s_lshl_b32 s0, s93, 4
	s_lshl_b32 s1, s91, 2
	s_add_i32 s2, s0, s1
	v_lshl_add_u64 v[0:1], s[86:87], 2, v[136:137]
	v_mad_i64_i32 v[2:3], s[0:1], s2, v133, v[0:1]
	s_or_b32 s0, s2, 1
	global_store_dwordx4 v[2:3], v[12:15], off
	v_mad_i64_i32 v[2:3], s[0:1], s0, v133, v[0:1]
	s_or_b32 s0, s2, 2
	global_store_dwordx4 v[2:3], v[16:19], off
	v_mad_i64_i32 v[2:3], s[0:1], s0, v133, v[0:1]
	s_or_b32 s0, s2, 3
	s_add_i32 s90, s90, s89
	v_mad_i64_i32 v[0:1], s[0:1], s0, v133, v[0:1]
	s_cmpk_gt_i32 s90, 0x5ff
	global_store_dwordx4 v[2:3], v[20:23], off
	global_store_dwordx4 v[0:1], v[8:11], off
	s_cbranch_scc0 .LBB0_17

; __device__ __forceinline__ void conv_load(const ConvSrc& c, int lane, f32x4 (&v)[8]) {
;     const float* src = c.W + (size_t)(8 * (lane >> 3)) * c.ldn + 4 * (lane & 7);
; #pragma unroll
;     for (int t = 0; t < 8; ++t) v[t] = __builtin_nontemporal_load((const f32x4*)(src + (size_t)t * c.ldn));
; }
; __device__ __forceinline__ void conv_store(const ConvSrc& c, int lane, f32x4 (&v)[8]) {
;     if (c.scale) { const f32x4 s0 = *(const f32x4*)(c.scale + 8 * (lane >> 3)), s1 = *(const f32x4*)(c.scale + 8 * (lane >> 3) + 4);
;         v[0] *= s0.x; v[1] *= s0.y; v[2] *= s0.z; v[3] *= s0.w; v[4] *= s1.x; v[5] *= s1.y; v[6] *= s1.z; v[7] *= s1.w; }
; template <int STREAM> __device__ __forceinline__ void conv_burst(Frame& F, const Args& A, int lane, int gw, int NGW, int& cur, int n) {
;     ...
;         const int i0 = gw + NGW * cur; if (i0 >= N) break;
;         const int i1 = i0 + NGW; const bool two = n > 1 && i1 < N;
;         const ConvSrc c0 = conv_item<STREAM>(A, F.ws, i0); f32x4 v0[8], v1[8];
;         conv_load(c0, lane, v0);
;         if (two) { const ConvSrc c1 = conv_item<STREAM>(A, F.ws, i1); conv_load(c1, lane, v1); conv_store(c0, lane, v0); conv_store(c1, lane, v1); cur += 2; n -= 2; }
;         else { conv_store(c0, lane, v0); cur += 1; n -= 1; }
.LBB0_37:
	s_add_i32 s29, s29, s89
	s_cmp_lg_u32 s26, 1
	s_cselect_b64 s[12:13], -1, 0
	s_cmpk_lt_i32 s29, 0x11c0
	s_cselect_b64 s[14:15], -1, 0
	s_lshl_b64 s[16:17], s[10:11], 2
	v_mul_lo_u32 v2, s11, v86
	v_mul_lo_u32 v3, s10, v87
	v_mad_u64_u32 v[0:1], s[10:11], s10, v86, 0
	v_add3_u32 v1, v1, v3, v2
	v_lshl_add_u64 v[0:1], v[0:1], 2, s[8:9]
	v_lshl_add_u64 v[0:1], v[0:1], 0, v[90:91]
	s_waitcnt vmcnt(6)
	v_lshl_add_u64 v[4:5], v[0:1], 0, s[16:17]
	global_load_dwordx4 v[0:3], v[0:1], off nt
	s_nop 0
	global_load_dwordx4 v[16:19], v[4:5], off nt
	v_lshl_add_u64 v[4:5], v[4:5], 0, s[16:17]
	s_waitcnt vmcnt(6)
	v_lshl_add_u64 v[8:9], v[4:5], 0, s[16:17]
	global_load_dwordx4 v[4:7], v[4:5], off nt
	s_nop 0
	global_load_dwordx4 v[20:23], v[8:9], off nt
	v_lshl_add_u64 v[8:9], v[8:9], 0, s[16:17]
	s_waitcnt vmcnt(6)
	v_lshl_add_u64 v[12:13], v[8:9], 0, s[16:17]
	global_load_dwordx4 v[8:11], v[8:9], off nt
	s_nop 0
	global_load_dwordx4 v[24:27], v[12:13], off nt
	v_lshl_add_u64 v[12:13], v[12:13], 0, s[16:17]
	s_waitcnt vmcnt(7)
	v_lshl_add_u64 v[28:29], v[12:13], 0, s[16:17]
	global_load_dwordx4 v[12:15], v[12:13], off nt
	s_nop 0
	global_load_dwordx4 v[28:31], v[28:29], off nt
	s_and_b64 s[8:9], s[12:13], s[14:15]
	s_andn2_b64 vcc, exec, s[8:9]
	s_mov_b64 s[8:9], -1
	s_cbranch_vccz .LBB0_42
	s_cmp_lg_u64 s[6:7], 0
	s_cbranch_scc0 .LBB0_62
	v_lshl_add_u64 v[32:33], v[86:87], 2, s[6:7]
	global_load_dwordx4 v[34:37], v[32:33], off nt
	global_load_dwordx4 v[38:41], v[32:33], off offset:16 nt
	s_waitcnt vmcnt(1)
	v_pk_mul_f32 v[54:55], v[6:7], v[36:37] op_sel_hi:[1,0]
	v_pk_mul_f32 v[72:73], v[4:5], v[36:37] op_sel_hi:[1,0]
	v_mov_b32_e32 v36, v37
	s_waitcnt vmcnt(0)
	v_pk_mul_f32 v[52:53], v[10:11], v[38:39] op_sel_hi:[1,0]
	v_pk_mul_f32 v[64:65], v[8:9], v[38:39] op_sel_hi:[1,0]
	v_pk_mul_f32 v[50:51], v[26:27], v[38:39] op_sel:[0,1]
	v_pk_mul_f32 v[32:33], v[24:25], v[38:39] op_sel:[0,1]
	v_mov_b32_e32 v38, v41
	v_pk_mul_f32 v[58:59], v[2:3], v[34:35] op_sel_hi:[1,0]
	v_pk_mul_f32 v[74:75], v[0:1], v[34:35] op_sel_hi:[1,0]
	v_pk_mul_f32 v[56:57], v[18:19], v[34:35] op_sel:[0,1]
	v_pk_mul_f32 v[34:35], v[16:17], v[34:35] op_sel:[0,1]
	v_pk_mul_f32 v[60:61], v[22:23], v[36:37] op_sel_hi:[1,0]
	v_pk_mul_f32 v[36:37], v[20:21], v[36:37] op_sel_hi:[1,0]
	v_pk_mul_f32 v[66:67], v[14:15], v[40:41] op_sel_hi:[1,0]
	v_mov_b64_e32 v[44:45], v[38:39]
	v_pk_mul_f32 v[62:63], v[12:13], v[40:41] op_sel_hi:[1,0]
	v_pk_mul_f32 v[70:71], v[30:31], v[38:39] op_sel_hi:[1,0]
	v_pk_mul_f32 v[68:69], v[28:29], v[38:39] op_sel_hi:[1,0]
	v_mov_b64_e32 v[48:49], v[36:37]
	v_mov_b64_e32 v[42:43], v[36:37]
	v_mov_b64_e32 v[40:41], v[34:35]
	v_mov_b64_e32 v[46:47], v[34:35]
	v_mov_b64_e32 v[38:39], v[32:33]
	s_cbranch_execnz .LBB0_41

; __device__ __forceinline__ void conv_load(const ConvSrc& c, int lane, f32x4 (&v)[8]) {
;     const float* src = c.W + (size_t)(8 * (lane >> 3)) * c.ldn + 4 * (lane & 7);
; #pragma unroll
;     for (int t = 0; t < 8; ++t) v[t] = __builtin_nontemporal_load((const f32x4*)(src + (size_t)t * c.ldn));
; }
; __device__ __forceinline__ void conv_store(const ConvSrc& c, int lane, f32x4 (&v)[8]) {
;     if (c.scale) { const f32x4 s0 = *(const f32x4*)(c.scale + 8 * (lane >> 3)), s1 = *(const f32x4*)(c.scale + 8 * (lane >> 3) + 4);
;         v[0] *= s0.x; v[1] *= s0.y; v[2] *= s0.z; v[3] *= s0.w; v[4] *= s1.x; v[5] *= s1.y; v[6] *= s1.z; v[7] *= s1.w; }
; template <int STREAM> __device__ __forceinline__ void conv_burst(Frame& F, const Args& A, int lane, int gw, int NGW, int& cur, int n) {
;     ...
;         const ConvSrc c0 = conv_item<STREAM>(A, F.ws, i0); f32x4 v0[8], v1[8];
;         conv_load(c0, lane, v0);
;         if (two) { const ConvSrc c1 = conv_item<STREAM>(A, F.ws, i1); conv_load(c1, lane, v1); conv_store(c0, lane, v0); conv_store(c1, lane, v1); cur += 2; n -= 2; }
.LBB0_54:
	v_mul_lo_u32 v34, s17, v86
	v_mul_lo_u32 v35, s16, v87
	v_mad_u64_u32 v[32:33], s[18:19], s16, v86, 0
	v_add3_u32 v33, v33, v35, v34
	v_lshl_add_u64 v[32:33], v[32:33], 2, s[14:15]
	v_lshl_add_u64 v[32:33], v[32:33], 0, v[90:91]
	s_lshl_b64 s[14:15], s[16:17], 2
	v_lshl_add_u64 v[36:37], v[32:33], 0, s[14:15]
	global_load_dwordx4 v[32:35], v[32:33], off nt
	s_nop 0
	global_load_dwordx4 v[40:43], v[36:37], off nt
	v_lshl_add_u64 v[36:37], v[36:37], 0, s[14:15]
	v_lshl_add_u64 v[44:45], v[36:37], 0, s[14:15]
	global_load_dwordx4 v[36:39], v[36:37], off nt
	s_nop 0
	global_load_dwordx4 v[48:51], v[44:45], off nt
	v_lshl_add_u64 v[44:45], v[44:45], 0, s[14:15]
	v_lshl_add_u64 v[56:57], v[44:45], 0, s[14:15]
	global_load_dwordx4 v[44:47], v[44:45], off nt
	s_nop 0
	global_load_dwordx4 v[52:55], v[56:57], off nt
	v_lshl_add_u64 v[56:57], v[56:57], 0, s[14:15]
	v_lshl_add_u64 v[60:61], v[56:57], 0, s[14:15]
	global_load_dwordx4 v[56:59], v[56:57], off nt
	s_nop 0
	global_load_dwordx4 v[60:63], v[60:61], off nt
	s_cmp_lg_u64 s[6:7], 0
	s_cbranch_scc0 .LBB0_63
	v_lshl_add_u64 v[64:65], v[86:87], 2, s[6:7]
	global_load_dwordx4 v[66:69], v[64:65], off nt
	global_load_dwordx4 v[70:73], v[64:65], off offset:16 nt
	s_waitcnt vmcnt(1)
	v_pk_mul_f32 v[6:7], v[6:7], v[68:69] op_sel_hi:[1,0]
	v_pk_mul_f32 v[100:101], v[4:5], v[68:69] op_sel_hi:[1,0]
	v_mov_b32_e32 v68, v69
	s_waitcnt vmcnt(0)
	v_mov_b32_e32 v74, v73
	v_pk_mul_f32 v[2:3], v[2:3], v[66:67] op_sel_hi:[1,0]
	v_pk_mul_f32 v[98:99], v[0:1], v[66:67] op_sel_hi:[1,0]
	v_pk_mul_f32 v[94:95], v[18:19], v[66:67] op_sel:[0,1]
	v_pk_mul_f32 v[66:67], v[16:17], v[66:67] op_sel:[0,1]
	v_pk_mul_f32 v[14:15], v[14:15], v[72:73] op_sel_hi:[1,0]
	v_pk_mul_f32 v[104:105], v[12:13], v[72:73] op_sel_hi:[1,0]
	v_pk_mul_f32 v[96:97], v[22:23], v[68:69] op_sel_hi:[1,0]
	v_pk_mul_f32 v[72:73], v[20:21], v[68:69] op_sel_hi:[1,0]
	v_pk_mul_f32 v[68:69], v[28:29], v[74:75] op_sel_hi:[1,0]
	v_mov_b64_e32 v[80:81], v[74:75]
	v_pk_mul_f32 v[10:11], v[10:11], v[70:71] op_sel_hi:[1,0]
	v_pk_mul_f32 v[102:103], v[8:9], v[70:71] op_sel_hi:[1,0]
	v_pk_mul_f32 v[92:93], v[26:27], v[70:71] op_sel:[0,1]
	v_pk_mul_f32 v[64:65], v[24:25], v[70:71] op_sel:[0,1]
	v_pk_mul_f32 v[70:71], v[30:31], v[74:75] op_sel_hi:[1,0]
	v_mov_b64_e32 v[84:85], v[68:69]
	v_mov_b64_e32 v[78:79], v[72:73]
	v_mov_b64_e32 v[76:77], v[66:67]
	v_mov_b32_e32 v13, v105
	v_mov_b32_e32 v9, v103
	v_mov_b32_e32 v5, v101
	v_mov_b32_e32 v1, v99
	v_mov_b64_e32 v[82:83], v[66:67]
	v_mov_b64_e32 v[74:75], v[64:65]
	s_cbranch_execnz .LBB0_57

; __device__ __forceinline__ unsigned pk2(float lo, float hi) { f32x2 v = {lo, hi}; bf16x2_t b = __builtin_convertvector(v, bf16x2_t); return __builtin_bit_cast(unsigned, b); }
; __device__ __forceinline__ void conv_store(const ConvSrc& c, int lane, f32x4 (&v)[8]) {
;     if (c.scale) { const f32x4 s0 = *(const f32x4*)(c.scale + 8 * (lane >> 3)), s1 = *(const f32x4*)(c.scale + 8 * (lane >> 3) + 4);
;         v[0] *= s0.x; v[1] *= s0.y; v[2] *= s0.z; v[3] *= s0.w; v[4] *= s1.x; v[5] *= s1.y; v[6] *= s1.z; v[7] *= s1.w; }
;     bf16* dst = c.WT + (size_t)(4 * (lane & 7)) * c.ldk + 8 * (lane >> 3);
; #pragma unroll
;     for (int j = 0; j < 4; ++j) { v4u o; o.x = pk2(v[0][j], v[1][j]); o.y = pk2(v[2][j], v[3][j]); o.z = pk2(v[4][j], v[5][j]); o.w = pk2(v[6][j], v[7][j]); __builtin_nontemporal_store(o, (v4u*)(dst + (size_t)j * c.ldk)); }
; }
; template <int STREAM> __device__ __forceinline__ void conv_burst(Frame& F, const Args& A, int lane, int gw, int NGW, int& cur, int n) {
;     ...
;         if (two) { const ConvSrc c1 = conv_item<STREAM>(A, F.ws, i1); conv_load(c1, lane, v1); conv_store(c0, lane, v0); conv_store(c1, lane, v1); cur += 2; n -= 2; }
.LBB0_57:
	v_mul_u32_u24_e32 v0, s4, v88
	v_lshlrev_b32_e32 v16, 1, v0
	v_mov_b32_e32 v17, v91
	v_lshl_add_u64 v[16:17], s[2:3], 0, v[16:17]
	v_lshl_add_u64 v[20:21], v[86:87], 1, v[16:17]
	v_cvt_pk_bf16_f32 v16, v98, v82
	v_cvt_pk_bf16_f32 v17, v100, v78
	v_cvt_pk_bf16_f32 v18, v102, v74
	v_cvt_pk_bf16_f32 v19, v104, v68
	s_lshl_b64 s[2:3], s[4:5], 1
	global_store_dwordx4 v[20:21], v[16:19], off nt
	s_cmp_lg_u64 s[12:13], 0
	s_nop 0
	v_cvt_pk_bf16_f32 v16, v1, v67
	v_cvt_pk_bf16_f32 v17, v5, v73
	v_cvt_pk_bf16_f32 v18, v9, v65
	s_waitcnt vmcnt(10)
	v_cvt_pk_bf16_f32 v19, v13, v69
	v_lshl_add_u64 v[0:1], v[20:21], 0, s[2:3]
	global_store_dwordx4 v[0:1], v[16:19], off nt
	v_lshl_add_u64 v[4:5], v[0:1], 0, s[2:3]
	v_cvt_pk_bf16_f32 v0, v3, v95
	v_cvt_pk_bf16_f32 v16, v2, v94
	v_cvt_pk_bf16_f32 v17, v6, v96
	v_cvt_pk_bf16_f32 v18, v10, v92
	v_cvt_pk_bf16_f32 v19, v14, v70
	global_store_dwordx4 v[4:5], v[16:19], off nt
	v_cvt_pk_bf16_f32 v1, v7, v97
	v_cvt_pk_bf16_f32 v2, v11, v93
	v_cvt_pk_bf16_f32 v3, v15, v71
	v_lshl_add_u64 v[4:5], v[4:5], 0, s[2:3]
	global_store_dwordx4 v[4:5], v[0:3], off nt
	s_cbranch_scc0 .LBB0_64
	s_nop 0
	v_lshl_add_u64 v[0:1], v[86:87], 2, s[12:13]
	global_load_dwordx4 v[10:13], v[0:1], off nt
	global_load_dwordx4 v[20:23], v[0:1], off offset:16 nt
	s_waitcnt vmcnt(1)
	v_mov_b32_e32 v24, v13
	s_waitcnt vmcnt(0)
	v_mov_b32_e32 v26, v23
	v_pk_mul_f32 v[2:3], v[34:35], v[10:11] op_sel_hi:[1,0]
	v_pk_mul_f32 v[0:1], v[32:33], v[10:11] op_sel_hi:[1,0]
	v_pk_mul_f32 v[6:7], v[42:43], v[10:11] op_sel:[0,1]
	v_pk_mul_f32 v[4:5], v[40:41], v[10:11] op_sel:[0,1]
	v_pk_mul_f32 v[10:11], v[38:39], v[12:13] op_sel_hi:[1,0]
	v_pk_mul_f32 v[8:9], v[36:37], v[12:13] op_sel_hi:[1,0]
	v_pk_mul_f32 v[14:15], v[46:47], v[20:21] op_sel_hi:[1,0]
	v_pk_mul_f32 v[12:13], v[44:45], v[20:21] op_sel_hi:[1,0]
	v_pk_mul_f32 v[18:19], v[54:55], v[20:21] op_sel:[0,1]
	v_pk_mul_f32 v[16:17], v[52:53], v[20:21] op_sel:[0,1]
	v_pk_mul_f32 v[66:67], v[58:59], v[22:23] op_sel_hi:[1,0]
	v_pk_mul_f32 v[64:65], v[56:57], v[22:23] op_sel_hi:[1,0]
	v_pk_mul_f32 v[22:23], v[50:51], v[24:25] op_sel_hi:[1,0]
	v_pk_mul_f32 v[20:21], v[48:49], v[24:25] op_sel_hi:[1,0]
	v_pk_mul_f32 v[70:71], v[62:63], v[26:27] op_sel_hi:[1,0]
	v_pk_mul_f32 v[68:69], v[60:61], v[26:27] op_sel_hi:[1,0]
	s_cbranch_execnz .LBB0_60

; __device__ __forceinline__ void conv_load(const ConvSrc& c, int lane, f32x4 (&v)[8]) {
;     const float* src = c.W + (size_t)(8 * (lane >> 3)) * c.ldn + 4 * (lane & 7);
; #pragma unroll
;     for (int t = 0; t < 8; ++t) v[t] = __builtin_nontemporal_load((const f32x4*)(src + (size_t)t * c.ldn));
; }
; __device__ __forceinline__ void conv_store(const ConvSrc& c, int lane, f32x4 (&v)[8]) {
;     if (c.scale) { const f32x4 s0 = *(const f32x4*)(c.scale + 8 * (lane >> 3)), s1 = *(const f32x4*)(c.scale + 8 * (lane >> 3) + 4);
;         v[0] *= s0.x; v[1] *= s0.y; v[2] *= s0.z; v[3] *= s0.w; v[4] *= s1.x; v[5] *= s1.y; v[6] *= s1.z; v[7] *= s1.w; }
; template <int STREAM> __device__ __forceinline__ void conv_burst(Frame& F, const Args& A, int lane, int gw, int NGW, int& cur, int n) {
;     ...
;         const int i0 = gw + NGW * cur; if (i0 >= N) break;
;         const int i1 = i0 + NGW; const bool two = n > 1 && i1 < N;
;         const ConvSrc c0 = conv_item<STREAM>(A, F.ws, i0); f32x4 v0[8], v1[8];
;         conv_load(c0, lane, v0);
;         if (two) { const ConvSrc c1 = conv_item<STREAM>(A, F.ws, i1); conv_load(c1, lane, v1); conv_store(c0, lane, v0); conv_store(c1, lane, v1); cur += 2; n -= 2; }
;         else { conv_store(c0, lane, v0); cur += 1; n -= 1; }
.LBB0_85:
	s_add_i32 s30, s30, s89
	s_cmp_lg_u32 s27, 1
	s_cselect_b64 s[12:13], -1, 0
	s_cmpk_lt_i32 s30, 0x11c0
	s_cselect_b64 s[14:15], -1, 0
	s_lshl_b64 s[16:17], s[10:11], 2
	v_mul_lo_u32 v2, s11, v86
	v_mul_lo_u32 v3, s10, v87
	v_mad_u64_u32 v[0:1], s[10:11], s10, v86, 0
	v_add3_u32 v1, v1, v3, v2
	v_lshl_add_u64 v[0:1], v[0:1], 2, s[8:9]
	v_lshl_add_u64 v[0:1], v[0:1], 0, v[90:91]
	s_waitcnt vmcnt(6)
	v_lshl_add_u64 v[4:5], v[0:1], 0, s[16:17]
	global_load_dwordx4 v[0:3], v[0:1], off nt
	s_nop 0
	global_load_dwordx4 v[16:19], v[4:5], off nt
	v_lshl_add_u64 v[4:5], v[4:5], 0, s[16:17]
	s_waitcnt vmcnt(6)
	v_lshl_add_u64 v[8:9], v[4:5], 0, s[16:17]
	global_load_dwordx4 v[4:7], v[4:5], off nt
	s_nop 0
	global_load_dwordx4 v[20:23], v[8:9], off nt
	v_lshl_add_u64 v[8:9], v[8:9], 0, s[16:17]
	s_waitcnt vmcnt(6)
	v_lshl_add_u64 v[12:13], v[8:9], 0, s[16:17]
	global_load_dwordx4 v[8:11], v[8:9], off nt
	s_nop 0
	global_load_dwordx4 v[24:27], v[12:13], off nt
	v_lshl_add_u64 v[12:13], v[12:13], 0, s[16:17]
	s_waitcnt vmcnt(7)
	v_lshl_add_u64 v[28:29], v[12:13], 0, s[16:17]
	global_load_dwordx4 v[12:15], v[12:13], off nt
	s_nop 0
	global_load_dwordx4 v[28:31], v[28:29], off nt
	s_and_b64 s[8:9], s[12:13], s[14:15]
	s_andn2_b64 vcc, exec, s[8:9]
	s_mov_b64 s[8:9], -1
	s_cbranch_vccz .LBB0_90
	s_cmp_lg_u64 s[6:7], 0
	s_cbranch_scc0 .LBB0_110
	v_lshl_add_u64 v[32:33], v[86:87], 2, s[6:7]
	global_load_dwordx4 v[34:37], v[32:33], off nt
	global_load_dwordx4 v[38:41], v[32:33], off offset:16 nt
	s_waitcnt vmcnt(1)
	v_pk_mul_f32 v[54:55], v[6:7], v[36:37] op_sel_hi:[1,0]
	v_pk_mul_f32 v[72:73], v[4:5], v[36:37] op_sel_hi:[1,0]
	v_mov_b32_e32 v36, v37
	s_waitcnt vmcnt(0)
	v_pk_mul_f32 v[52:53], v[10:11], v[38:39] op_sel_hi:[1,0]
	v_pk_mul_f32 v[64:65], v[8:9], v[38:39] op_sel_hi:[1,0]
	v_pk_mul_f32 v[50:51], v[26:27], v[38:39] op_sel:[0,1]
	v_pk_mul_f32 v[32:33], v[24:25], v[38:39] op_sel:[0,1]
	v_mov_b32_e32 v38, v41
	v_pk_mul_f32 v[58:59], v[2:3], v[34:35] op_sel_hi:[1,0]
	v_pk_mul_f32 v[74:75], v[0:1], v[34:35] op_sel_hi:[1,0]
	v_pk_mul_f32 v[56:57], v[18:19], v[34:35] op_sel:[0,1]
	v_pk_mul_f32 v[34:35], v[16:17], v[34:35] op_sel:[0,1]
	v_pk_mul_f32 v[60:61], v[22:23], v[36:37] op_sel_hi:[1,0]
	v_pk_mul_f32 v[36:37], v[20:21], v[36:37] op_sel_hi:[1,0]
	v_pk_mul_f32 v[66:67], v[14:15], v[40:41] op_sel_hi:[1,0]
	v_mov_b64_e32 v[44:45], v[38:39]
	v_pk_mul_f32 v[62:63], v[12:13], v[40:41] op_sel_hi:[1,0]
	v_pk_mul_f32 v[70:71], v[30:31], v[38:39] op_sel_hi:[1,0]
	v_pk_mul_f32 v[68:69], v[28:29], v[38:39] op_sel_hi:[1,0]
	v_mov_b64_e32 v[48:49], v[36:37]
	v_mov_b64_e32 v[42:43], v[36:37]
	v_mov_b64_e32 v[40:41], v[34:35]
	v_mov_b64_e32 v[46:47], v[34:35]
	v_mov_b64_e32 v[38:39], v[32:33]
	s_cbranch_execnz .LBB0_89
